# conversion split: P4 fill 9 tiles per workgroup, P5 26; P3/P4 tile ranges shifted up by 256
# baseline (speedup 1.0000x reference)
; __device__ __forceinline__ void conv8_fill(const Ctx& X, int base, int rank, int nblk, int n) { conv8b_run(X, (base >> 3) + rank, nblk, n); }
; #define SEAM(k) do { if (IN(k) && IN((k) + 1)) xcd_barrier(bar); } while (0)
; __device__ __forceinline__ Cvb conv8b_dec(const Ctx& X, int bit) { Cvb c; int kb, nb;
;     if (bit < I_GU8 / 8) { const int e = bit >> 8, r = bit & 255; kb = r >> 4; nb = r & 15; c.N = 2 * DFF; c.W = XP_w_gu(X) + (size_t)e * D * (2 * DFF); c.WT = XP_WguT(X) + (size_t)e * 16 * PAN_GU + (size_t)kb * PAN_GU; }
;     else { const int b2 = bit - I_GU8 / 8, e = b2 >> 7, r = b2 & 127; kb = r >> 3; nb = r & 7; c.N = D; c.W = XP_w_d(X) + (size_t)e * DFF * D; c.WT = XP_WdT(X) + (size_t)e * 16 * PAN_D + (size_t)kb * PAN_D; }
;     c.W += (size_t)(kb * 128 + 16 * X.wave) * c.N + nb * 256 + 4 * X.lane;
;     c.WT += (size_t)(nb * 256 + 32 * X.wave + (X.lane >> 3)) * 128 + 16 * (X.lane & 7);
;     return c; }
; __device__ __forceinline__ void conv8b_run(const Ctx& X, int first, int step, int count) {
;     if (count <= 0) return;
;     f32x4 v[16];
;     Cvb c = conv8b_dec(X, first), cn = c;
; #pragma unroll
;     for (int i = 0; i < 16; ++i) v[i] = __builtin_nontemporal_load((const f32x4*)(c.W + (size_t)i * c.N));
; __global__ void __launch_bounds__(NTHR, 2) fwd(Args args) {
;     ...
;     if (IN(3)) { p3_scan(X); if (X.G == 256 && X.bid >= 192) conv8_fill(X, FILL_B3, X.bid - 192, FILL_W3 / NWAVES, FILL_N3); } SEAM(3);
.LBB0_474:
	s_or_b64 exec, exec, s[6:7]
	s_cmpk_lg_i32 s92, 0x100
	s_cselect_b64 s[2:3], -1, 0
	s_cmpk_lt_i32 s87, 0xc0
	s_cselect_b64 s[6:7], -1, 0
	s_or_b64 s[2:3], s[6:7], s[2:3]
	s_and_b64 vcc, exec, s[2:3]
	s_cbranch_vccnz .LBB0_480
	s_load_dwordx2 s[6:7], s[0:1], 0x80
	s_add_i32 s2, s87, 0xa00
	s_lshr_b32 s2, s2, 7
	s_mov_b32 s3, 0
	s_bfe_u32 s13, s87, 0x40003
	s_lshl_b64 s[8:9], s[2:3], 24
	s_waitcnt lgkmcnt(0)
	s_mov_b64 s[100:101], s[6:7]
	s_add_u32 s14, s6, s8
	s_addc_u32 s15, s7, s9
	s_add_u32 s10, s90, 0x50000000
	s_addc_u32 s11, s91, 0
	s_lshl_b64 s[6:7], s[2:3], 22
	s_add_u32 s2, s10, s6
	s_addc_u32 s7, s11, s7
	s_lshl_b32 s6, s13, 18
	s_add_u32 s6, s2, s6
	s_addc_u32 s7, s7, 0
	s_lshl_b32 s2, s87, 8
	s_lshl_b32 s16, s93, 5
	s_and_b32 s17, s2, 0x700
	s_add_i32 s2, s16, s17
	v_lshrrev_b32_e32 v75, 3, v194
	v_or_b32_e32 v66, s2, v75
	s_lshl_b32 s12, s93, 4
	s_lshl_b32 s2, s13, 7
	s_add_i32 s2, s12, s2
	s_lshl_b64 s[8:9], s[2:3], 13
	s_add_u32 s2, s14, s8
	s_addc_u32 s9, s15, s9
	s_lshl_b32 s8, s17, 2
	v_mov_b32_e32 v67, 0
	s_add_u32 s8, s2, s8
	v_lshlrev_b64 v[68:69], 7, v[66:67]
	s_addc_u32 s9, s9, 0
	v_lshlrev_b32_e32 v66, 4, v194
	s_waitcnt vmcnt(3)
	v_lshl_add_u64 v[30:31], s[8:9], 0, v[66:67]
	s_mov_b32 s2, 0x1e000
	v_add_co_u32_e32 v6, vcc, s2, v30
	s_mov_b32 s2, 0x1c000
	s_nop 0
	v_addc_co_u32_e32 v7, vcc, 0, v31, vcc
	v_add_co_u32_e32 v8, vcc, s2, v30
	s_mov_b32 s2, 0x1a000
	s_nop 0
	v_addc_co_u32_e32 v9, vcc, 0, v31, vcc
	v_add_co_u32_e32 v10, vcc, s2, v30
	s_mov_b32 s2, 0x18000
	s_nop 0
	v_addc_co_u32_e32 v11, vcc, 0, v31, vcc
	v_add_co_u32_e32 v12, vcc, s2, v30
	s_mov_b32 s2, 0x16000
	s_nop 0
	v_addc_co_u32_e32 v13, vcc, 0, v31, vcc
	v_add_co_u32_e32 v14, vcc, s2, v30
	s_mov_b32 s2, 0x14000
	s_nop 0
	v_addc_co_u32_e32 v15, vcc, 0, v31, vcc
	v_add_co_u32_e32 v16, vcc, s2, v30
	s_mov_b32 s2, 0x12000
	s_nop 0
	v_addc_co_u32_e32 v17, vcc, 0, v31, vcc
	v_add_co_u32_e32 v18, vcc, s2, v30
	s_mov_b32 s2, 0x10000
	s_nop 0
	v_addc_co_u32_e32 v19, vcc, 0, v31, vcc
	v_add_co_u32_e32 v20, vcc, s2, v30
	s_mov_b32 s2, 0xe000
	s_nop 0
	v_addc_co_u32_e32 v21, vcc, 0, v31, vcc
	v_add_co_u32_e32 v22, vcc, s2, v30
	s_mov_b32 s2, 0xc000
	s_nop 0
	v_addc_co_u32_e32 v23, vcc, 0, v31, vcc
	v_add_co_u32_e32 v24, vcc, s2, v30
	s_mov_b32 s2, 0xa000
	s_nop 0
	v_addc_co_u32_e32 v25, vcc, 0, v31, vcc
	v_add_co_u32_e32 v26, vcc, s2, v30
	s_mov_b32 s2, 0x8000
	s_nop 0
	v_addc_co_u32_e32 v27, vcc, 0, v31, vcc
	v_add_co_u32_e32 v28, vcc, s2, v30
	s_movk_i32 s2, 0x6000
	s_nop 0
	v_addc_co_u32_e32 v29, vcc, 0, v31, vcc
	v_add_co_u32_e32 v32, vcc, s2, v30
	s_movk_i32 s2, 0x4000
	s_nop 0
	v_addc_co_u32_e32 v33, vcc, 0, v31, vcc
	s_waitcnt vmcnt(0)
	v_add_co_u32_e32 v62, vcc, s2, v30
	s_movk_i32 s2, 0x2000
	s_nop 0
	v_addc_co_u32_e32 v63, vcc, 0, v31, vcc
	v_add_co_u32_e32 v70, vcc, s2, v30
	global_load_dwordx4 v[34:37], v[6:7], off nt
	global_load_dwordx4 v[2:5], v[8:9], off nt
	v_addc_co_u32_e32 v71, vcc, 0, v31, vcc
	global_load_dwordx4 v[38:41], v[10:11], off nt
	global_load_dwordx4 v[6:9], v[12:13], off nt
	global_load_dwordx4 v[42:45], v[14:15], off nt
	s_nop 0
	global_load_dwordx4 v[10:13], v[16:17], off nt
	global_load_dwordx4 v[46:49], v[18:19], off nt
	s_nop 0
	global_load_dwordx4 v[14:17], v[20:21], off nt
	global_load_dwordx4 v[50:53], v[22:23], off nt
	s_nop 0
	global_load_dwordx4 v[18:21], v[24:25], off nt
	global_load_dwordx4 v[54:57], v[26:27], off nt
	s_nop 0
	global_load_dwordx4 v[22:25], v[28:29], off nt
	global_load_dwordx4 v[58:61], v[32:33], off nt
	s_nop 0
	global_load_dwordx4 v[26:29], v[62:63], off nt
	global_load_dwordx4 v[30:33], v[70:71], off nt
	s_nop 0
	global_load_dwordx4 v[62:65], v66, s[8:9] nt
	v_lshlrev_b32_e32 v66, 4, v0
	v_lshl_add_u64 v[70:71], s[6:7], 0, v[68:69]
	v_and_b32_e32 v68, 0x70, v66
	v_mov_b32_e32 v69, v67
	v_or_b32_e32 v66, s16, v75
	s_movk_i32 s2, 0x90
	v_lshl_add_u64 v[72:73], v[70:71], 0, v[68:69]
	v_lshlrev_b32_e32 v74, 2, v194
	v_mul_lo_u32 v77, v66, s2
	v_add_u32_e32 v66, s17, v66
	v_mul_u32_u24_e32 v76, 0x240, v194
	v_lshlrev_b64 v[70:71], 7, v[66:67]
	s_add_i32 s13, s87, 0x2a40
	s_mov_b32 s14, 0xc3e00000
	s_lshl_b32 s15, s17, 2
	v_lshlrev_b32_e32 v66, 2, v74
	v_mov_b32_e32 v78, 0x43e00000
	s_mov_b32 s16, 0
	v_mov_b64_e32 v[74:75], v[72:73]
	s_waitcnt vmcnt(0)
	s_branch .LBB0_477

; __device__ __forceinline__ void conv8_fill(const Ctx& X, int base, int rank, int nblk, int n) { conv8b_run(X, (base >> 3) + rank, nblk, n); }
; #define SEAM(k) do { if (IN(k) && IN((k) + 1)) xcd_barrier(bar); } while (0)
; __device__ __forceinline__ Cvb conv8b_dec(const Ctx& X, int bit) { Cvb c; int kb, nb;
;     if (bit < I_GU8 / 8) { const int e = bit >> 8, r = bit & 255; kb = r >> 4; nb = r & 15; c.N = 2 * DFF; c.W = XP_w_gu(X) + (size_t)e * D * (2 * DFF); c.WT = XP_WguT(X) + (size_t)e * 16 * PAN_GU + (size_t)kb * PAN_GU; }
;     else { const int b2 = bit - I_GU8 / 8, e = b2 >> 7, r = b2 & 127; kb = r >> 3; nb = r & 7; c.N = D; c.W = XP_w_d(X) + (size_t)e * DFF * D; c.WT = XP_WdT(X) + (size_t)e * 16 * PAN_D + (size_t)kb * PAN_D; }
;     c.W += (size_t)(kb * 128 + 16 * X.wave) * c.N + nb * 256 + 4 * X.lane;
;     c.WT += (size_t)(nb * 256 + 32 * X.wave + (X.lane >> 3)) * 128 + 16 * (X.lane & 7);
;     return c; }
; __device__ __forceinline__ void conv8b_run(const Ctx& X, int first, int step, int count) {
;     if (count <= 0) return;
;     f32x4 v[16];
;     Cvb c = conv8b_dec(X, first), cn = c;
; #pragma unroll
;     for (int i = 0; i < 16; ++i) v[i] = __builtin_nontemporal_load((const f32x4*)(c.W + (size_t)i * c.N));
; __global__ void __launch_bounds__(NTHR, 2) fwd(Args args) {
;     ...
;         if (X.G == 256 && X.bid >= 128) conv8_fill(X, FILL_B4, X.bid - 128, FILL_W4 / NWAVES, FILL_N4); } SEAM(4);
.LBB0_661:
	s_waitcnt lgkmcnt(0)
	s_cmpk_eq_i32 s92, 0x100
	v_readlane_b32 s87, v248, 9
	s_load_dwordx2 s[94:95], s[0:1], 0xa8
	s_cselect_b64 s[2:3], -1, 0
	s_cmpk_gt_i32 s87, 0x7f
	s_cselect_b64 s[4:5], -1, 0
	s_and_b64 s[2:3], s[4:5], s[2:3]
	v_readlane_b32 s96, v248, 7
	v_readlane_b32 s64, v248, 10
	v_readlane_b32 s30, v248, 5
	s_and_b64 vcc, exec, s[2:3]
	v_readlane_b32 s97, v248, 8
	v_readlane_b32 s61, v248, 2
	v_readlane_b32 s62, v248, 3
	v_readlane_b32 s65, v248, 11
	v_readlane_b32 s31, v248, 6
	s_cbranch_vccz .LBB0_671
	s_load_dwordx2 s[4:5], s[0:1], 0x80
	s_add_i32 s2, s87, 0xb00
	s_lshr_b32 s2, s2, 7
	s_mov_b32 s3, 0
	s_bfe_u32 s8, s87, 0x40003
	s_lshl_b64 s[6:7], s[2:3], 24
	s_waitcnt lgkmcnt(0)
	s_mov_b64 s[100:101], s[4:5]
	s_add_u32 s10, s4, s6
	s_addc_u32 s11, s5, s7
	s_add_u32 s18, s90, 0x50000000
	s_addc_u32 s19, s91, 0
	s_lshl_b64 s[4:5], s[2:3], 22
	s_add_u32 s6, s18, s4
	s_addc_u32 s7, s19, s5
	s_lshl_b32 s2, s8, 18
	s_add_u32 s6, s6, s2
	s_mov_b64 s[4:5], s[2:3]
	s_addc_u32 s7, s7, 0
	s_lshl_b32 s2, s87, 8
	s_lshl_b32 s12, s93, 5
	s_and_b32 s13, s2, 0x700
	s_add_i32 s2, s12, s13
	v_lshrrev_b32_e32 v72, 3, v194
	v_or_b32_e32 v66, s2, v72
	s_lshl_b32 s20, s93, 4
	s_lshl_b32 s2, s8, 7
	s_add_i32 s2, s20, s2
	s_lshl_b64 s[8:9], s[2:3], 13
	s_add_u32 s8, s10, s8
	s_addc_u32 s9, s11, s9
	s_lshl_b32 s10, s13, 2
	v_mov_b32_e32 v67, 0
	s_add_u32 s8, s8, s10
	v_lshlrev_b64 v[68:69], 7, v[66:67]
	s_addc_u32 s9, s9, 0
	v_lshlrev_b32_e32 v66, 4, v194
	s_waitcnt vmcnt(2)
	v_lshl_add_u64 v[54:55], s[8:9], 0, v[66:67]
	s_mov_b32 s10, 0x1e000
	v_add_co_u32_e32 v10, vcc, s10, v54
	s_mov_b32 s10, 0x1c000
	s_nop 0
	v_addc_co_u32_e32 v11, vcc, 0, v55, vcc
	v_add_co_u32_e32 v12, vcc, s10, v54
	s_mov_b32 s10, 0x1a000
	s_nop 0
	v_addc_co_u32_e32 v13, vcc, 0, v55, vcc
	v_add_co_u32_e32 v18, vcc, s10, v54
	s_mov_b32 s10, 0x18000
	s_nop 0
	v_addc_co_u32_e32 v19, vcc, 0, v55, vcc
	v_add_co_u32_e32 v20, vcc, s10, v54
	s_mov_b32 s10, 0x16000
	s_nop 0
	v_addc_co_u32_e32 v21, vcc, 0, v55, vcc
	v_add_co_u32_e32 v26, vcc, s10, v54
	s_mov_b32 s10, 0x14000
	s_nop 0
	v_addc_co_u32_e32 v27, vcc, 0, v55, vcc
	v_add_co_u32_e32 v28, vcc, s10, v54
	s_mov_b32 s10, 0x12000
	s_nop 0
	v_addc_co_u32_e32 v29, vcc, 0, v55, vcc
	v_add_co_u32_e32 v34, vcc, s10, v54
	s_mov_b32 s10, 0x10000
	s_nop 0
	v_addc_co_u32_e32 v35, vcc, 0, v55, vcc
	v_add_co_u32_e32 v36, vcc, s10, v54
	s_mov_b32 s10, 0xe000
	s_nop 0
	v_addc_co_u32_e32 v37, vcc, 0, v55, vcc
	s_waitcnt vmcnt(1)
	v_add_co_u32_e32 v42, vcc, s10, v54
	s_mov_b32 s10, 0xc000
	s_nop 0
	v_addc_co_u32_e32 v43, vcc, 0, v55, vcc
	v_add_co_u32_e32 v44, vcc, s10, v54
	s_mov_b32 s10, 0xa000
	s_nop 0
	v_addc_co_u32_e32 v45, vcc, 0, v55, vcc
	s_waitcnt vmcnt(0)
	v_add_co_u32_e32 v50, vcc, s10, v54
	s_mov_b32 s10, 0x8000
	s_nop 0
	v_addc_co_u32_e32 v51, vcc, 0, v55, vcc
	v_add_co_u32_e32 v52, vcc, s10, v54
	s_movk_i32 s10, 0x6000
	s_nop 0
	v_addc_co_u32_e32 v53, vcc, 0, v55, vcc
	v_add_co_u32_e32 v56, vcc, s10, v54
	s_movk_i32 s10, 0x4000
	s_nop 0
	v_addc_co_u32_e32 v57, vcc, 0, v55, vcc
	v_add_co_u32_e32 v62, vcc, s10, v54
	s_movk_i32 s10, 0x2000
	s_nop 0
	v_addc_co_u32_e32 v63, vcc, 0, v55, vcc
	v_add_co_u32_e32 v70, vcc, s10, v54
	global_load_dwordx4 v[2:5], v[10:11], off nt
	global_load_dwordx4 v[6:9], v[12:13], off nt
	v_addc_co_u32_e32 v71, vcc, 0, v55, vcc
	global_load_dwordx4 v[10:13], v[18:19], off nt
	global_load_dwordx4 v[14:17], v[20:21], off nt
	s_nop 0
	global_load_dwordx4 v[18:21], v[26:27], off nt
	global_load_dwordx4 v[22:25], v[28:29], off nt
	s_nop 0
	global_load_dwordx4 v[26:29], v[34:35], off nt
	global_load_dwordx4 v[30:33], v[36:37], off nt
	global_load_dwordx4 v[38:41], v[42:43], off nt
	s_nop 0
	global_load_dwordx4 v[34:37], v[44:45], off nt
	global_load_dwordx4 v[46:49], v[50:51], off nt
	s_nop 0
	global_load_dwordx4 v[42:45], v[52:53], off nt
	global_load_dwordx4 v[58:61], v[56:57], off nt
	s_nop 0
	global_load_dwordx4 v[50:53], v[62:63], off nt
	s_nop 0
	global_load_dwordx4 v[62:65], v[70:71], off nt
	global_load_dwordx4 v[54:57], v66, s[8:9] nt
	v_lshlrev_b32_e32 v66, 4, v0
	v_lshl_add_u64 v[70:71], s[6:7], 0, v[68:69]
	v_and_b32_e32 v68, 0x70, v66
	v_mov_b32_e32 v69, v67
	s_and_b32 s21, s87, 7
	s_and_b32 s22, s87, 15
	v_lshl_add_u64 v[70:71], v[70:71], 0, v[68:69]
	s_mov_b64 s[6:7], s[2:3]
	v_lshlrev_b32_e32 v66, 2, v194
	v_or_b32_e32 v75, s12, v72
	s_add_u32 s23, s90, 0x30000000
	s_movk_i32 s2, 0x90
	v_mul_u32_u24_e32 v74, 0x240, v194
	s_addc_u32 s24, s91, 0
	v_mul_lo_u32 v76, v75, s2
	s_add_i32 s25, s87, 0x2b80
	s_mov_b32 s26, 0xc3e00000
	v_lshlrev_b32_e32 v66, 2, v66
	v_mov_b32_e32 v77, 0x43e00000
	s_mov_b32 s27, 0
	v_mov_b64_e32 v[72:73], v[70:71]
	s_waitcnt vmcnt(0)
	s_branch .LBB0_665

; #define LAS __attribute__((address_space(3)))
; __device__ __forceinline__ void conv8b_run(const Ctx& X, int first, int step, int count) {
;     ...
;         asm volatile("s_waitcnt lgkmcnt(0)" ::: "memory"); __builtin_amdgcn_s_barrier();
; #pragma unroll
;         for (int it = 0; it < 4; ++it) { const u32x4 r = *(const LAS u32x4*)(buf + (32 * X.wave + 8 * it + (X.lane >> 3)) * CVT_STRIDE + 16 * (X.lane & 7));
;             __builtin_nontemporal_store(r, (u32x4*)(c.WT + (size_t)it * 8 * 128)); }
;         c = cn;
.LBB0_664:
	v_add3_u32 v90, s28, v76, v68
	s_waitcnt lgkmcnt(0)
	s_barrier
	ds_read_b128 v[78:81], v90
	ds_read_b128 v[82:85], v90 offset:1152
	ds_read_b128 v[86:89], v90 offset:2304
	ds_read_b128 v[90:93], v90 offset:3456
	s_add_i32 s27, s27, 1
	s_addk_i32 s25, 0x80
	s_waitcnt lgkmcnt(3)
	global_store_dwordx4 v[70:71], v[78:81], off nt
	s_waitcnt lgkmcnt(2)
	global_store_dwordx4 v[70:71], v[82:85], off offset:1024 nt
	s_waitcnt lgkmcnt(1)
	global_store_dwordx4 v[70:71], v[86:89], off offset:2048 nt
	s_waitcnt lgkmcnt(0)
	global_store_dwordx4 v[70:71], v[90:93], off offset:3072 nt
	s_cmp_lg_u32 s27, 9
	v_mov_b64_e32 v[70:71], v[72:73]
	s_cbranch_scc0 .LBB0_670
; #define LAS __attribute__((address_space(3)))
; __device__ __forceinline__ void conv8b_run(const Ctx& X, int first, int step, int count) {
;     ...
;     for (int j = 0; j < count; ++j) {
;         LAS uchar* buf = X.lds + (j & 1) * CVT_BUF;
; #pragma unroll
;         for (int q = 0; q < 4; ++q) { u32x4 o;
;             o.x = pk_fp8x4(v[0][q] * W8_SCALE, v[1][q] * W8_SCALE, v[2][q] * W8_SCALE, v[3][q] * W8_SCALE); o.y = pk_fp8x4(v[4][q] * W8_SCALE, v[5][q] * W8_SCALE, v[6][q] * W8_SCALE, v[7][q] * W8_SCALE);
;             o.z = pk_fp8x4(v[8][q] * W8_SCALE, v[9][q] * W8_SCALE, v[10][q] * W8_SCALE, v[11][q] * W8_SCALE); o.w = pk_fp8x4(v[12][q] * W8_SCALE, v[13][q] * W8_SCALE, v[14][q] * W8_SCALE, v[15][q] * W8_SCALE);
;             *(LAS u32x4*)(buf + (4 * X.lane + q) * CVT_STRIDE + 16 * X.wave) = o; }
;         if (j + 1 < count) { cn = conv8b_dec(X, first + (j + 1) * step);
; #pragma unroll
;             for (int i = 0; i < 16; ++i) v[i] = __builtin_nontemporal_load((const f32x4*)(cn.W + (size_t)i * cn.N)); }
.LBB0_665:
	s_waitcnt vmcnt(4)
	v_mul_f32_e32 v78, 0x42800000, v54
	v_mul_f32_e32 v79, 0x42800000, v62
	v_med3_f32 v81, v78, s26, v77
	v_med3_f32 v79, v79, s26, v77
	v_mov_b32_e32 v78, 0
	v_cvt_pk_fp8_f32 v78, v81, v79
	v_mul_f32_e32 v80, 0x42800000, v50
	v_mul_f32_e32 v79, 0x42800000, v58
	v_med3_f32 v80, v80, s26, v77
	v_med3_f32 v79, v79, s26, v77
	v_cvt_pk_fp8_f32 v78, v80, v79 op_sel:[0,0,1]
	v_mul_f32_e32 v79, 0x42800000, v42
	v_mul_f32_e32 v80, 0x42800000, v46
	v_med3_f32 v82, v79, s26, v77
	v_med3_f32 v80, v80, s26, v77
	v_mov_b32_e32 v79, 0
	v_cvt_pk_fp8_f32 v79, v82, v80
	v_mul_f32_e32 v81, 0x42800000, v34
	v_mul_f32_e32 v80, 0x42800000, v38
	v_med3_f32 v81, v81, s26, v77
	v_med3_f32 v80, v80, s26, v77
	v_cvt_pk_fp8_f32 v79, v81, v80 op_sel:[0,0,1]
	v_mul_f32_e32 v80, 0x42800000, v30
	v_mul_f32_e32 v81, 0x42800000, v26
	v_med3_f32 v83, v80, s26, v77
	v_med3_f32 v81, v81, s26, v77
	v_mov_b32_e32 v80, 0
	v_cvt_pk_fp8_f32 v80, v83, v81
	v_mul_f32_e32 v82, 0x42800000, v22
	v_mul_f32_e32 v81, 0x42800000, v18
	v_med3_f32 v82, v82, s26, v77
	v_med3_f32 v81, v81, s26, v77
	v_cvt_pk_fp8_f32 v80, v82, v81 op_sel:[0,0,1]
	v_mul_f32_e32 v81, 0x42800000, v14
	v_mul_f32_e32 v82, 0x42800000, v10
	v_med3_f32 v84, v81, s26, v77
	v_med3_f32 v82, v82, s26, v77
	v_mov_b32_e32 v81, 0
	v_cvt_pk_fp8_f32 v81, v84, v82
	v_mul_f32_e32 v83, 0x42800000, v6
	v_mul_f32_e32 v82, 0x42800000, v2
	s_bitcmp1_b32 s27, 0
	v_med3_f32 v83, v83, s26, v77
	v_med3_f32 v82, v82, s26, v77
	s_cselect_b32 s2, 0x9000, 0
	v_cvt_pk_fp8_f32 v81, v83, v82 op_sel:[0,0,1]
	s_add_i32 s28, s2, 0
	s_add_i32 s2, s20, s28
	v_add_u32_e32 v90, s2, v74
	ds_write_b128 v90, v[78:81]
	v_mul_f32_e32 v78, 0x42800000, v55
	v_mul_f32_e32 v79, 0x42800000, v63
	v_med3_f32 v81, v78, s26, v77
	v_med3_f32 v79, v79, s26, v77
	v_mov_b32_e32 v78, 0
	v_cvt_pk_fp8_f32 v78, v81, v79
	v_mul_f32_e32 v80, 0x42800000, v51
	v_mul_f32_e32 v79, 0x42800000, v59
	v_med3_f32 v80, v80, s26, v77
	v_med3_f32 v79, v79, s26, v77
	v_cvt_pk_fp8_f32 v78, v80, v79 op_sel:[0,0,1]
	v_mul_f32_e32 v79, 0x42800000, v43
	v_mul_f32_e32 v80, 0x42800000, v47
	v_med3_f32 v82, v79, s26, v77
	v_med3_f32 v80, v80, s26, v77
	v_mov_b32_e32 v79, 0
	v_cvt_pk_fp8_f32 v79, v82, v80
	v_mul_f32_e32 v81, 0x42800000, v35
	v_mul_f32_e32 v80, 0x42800000, v39
	v_med3_f32 v81, v81, s26, v77
	v_med3_f32 v80, v80, s26, v77
	v_cvt_pk_fp8_f32 v79, v81, v80 op_sel:[0,0,1]
	v_mul_f32_e32 v80, 0x42800000, v31
	v_mul_f32_e32 v81, 0x42800000, v27
	v_med3_f32 v83, v80, s26, v77
	v_med3_f32 v81, v81, s26, v77
	v_mov_b32_e32 v80, 0
	v_cvt_pk_fp8_f32 v80, v83, v81
	v_mul_f32_e32 v82, 0x42800000, v23
	v_mul_f32_e32 v81, 0x42800000, v19
	v_med3_f32 v82, v82, s26, v77
	v_med3_f32 v81, v81, s26, v77
	v_cvt_pk_fp8_f32 v80, v82, v81 op_sel:[0,0,1]
	v_mul_f32_e32 v81, 0x42800000, v15
	v_mul_f32_e32 v82, 0x42800000, v11
	v_med3_f32 v84, v81, s26, v77
	v_med3_f32 v82, v82, s26, v77
	v_mov_b32_e32 v81, 0
	v_cvt_pk_fp8_f32 v81, v84, v82
	v_mul_f32_e32 v83, 0x42800000, v7
	v_mul_f32_e32 v82, 0x42800000, v3
	v_med3_f32 v83, v83, s26, v77
	v_med3_f32 v82, v82, s26, v77
	v_cvt_pk_fp8_f32 v81, v83, v82 op_sel:[0,0,1]
	v_mul_f32_e32 v82, 0x42800000, v56
	v_mul_f32_e32 v83, 0x42800000, v64
	v_med3_f32 v85, v82, s26, v77
	v_med3_f32 v83, v83, s26, v77
	v_mov_b32_e32 v82, 0
	v_cvt_pk_fp8_f32 v82, v85, v83
	v_mul_f32_e32 v84, 0x42800000, v52
	v_mul_f32_e32 v83, 0x42800000, v60
	v_med3_f32 v84, v84, s26, v77
	v_med3_f32 v83, v83, s26, v77
	v_cvt_pk_fp8_f32 v82, v84, v83 op_sel:[0,0,1]
	v_mul_f32_e32 v83, 0x42800000, v44
	v_mul_f32_e32 v84, 0x42800000, v48
	v_med3_f32 v86, v83, s26, v77
	v_med3_f32 v84, v84, s26, v77
	v_mov_b32_e32 v83, 0
	v_cvt_pk_fp8_f32 v83, v86, v84
	v_mul_f32_e32 v85, 0x42800000, v36
	v_mul_f32_e32 v84, 0x42800000, v40
	v_med3_f32 v85, v85, s26, v77
	v_med3_f32 v84, v84, s26, v77
	v_cvt_pk_fp8_f32 v83, v85, v84 op_sel:[0,0,1]
	v_mul_f32_e32 v84, 0x42800000, v32
	v_mul_f32_e32 v85, 0x42800000, v28
	v_med3_f32 v87, v84, s26, v77
	v_med3_f32 v85, v85, s26, v77
	v_mov_b32_e32 v84, 0
	v_cvt_pk_fp8_f32 v84, v87, v85
	v_mul_f32_e32 v86, 0x42800000, v24
	v_mul_f32_e32 v85, 0x42800000, v20
	v_med3_f32 v86, v86, s26, v77
	v_med3_f32 v85, v85, s26, v77
	v_cvt_pk_fp8_f32 v84, v86, v85 op_sel:[0,0,1]
	v_mul_f32_e32 v85, 0x42800000, v16
	v_mul_f32_e32 v86, 0x42800000, v12
	v_med3_f32 v88, v85, s26, v77
	v_med3_f32 v86, v86, s26, v77
	v_mov_b32_e32 v85, 0
	v_cvt_pk_fp8_f32 v85, v88, v86
	v_mul_f32_e32 v87, 0x42800000, v8
	v_mul_f32_e32 v86, 0x42800000, v4
	v_med3_f32 v87, v87, s26, v77
	v_med3_f32 v86, v86, s26, v77
	v_cvt_pk_fp8_f32 v85, v87, v86 op_sel:[0,0,1]
	v_mul_f32_e32 v86, 0x42800000, v57
	v_mul_f32_e32 v87, 0x42800000, v65
	v_med3_f32 v89, v86, s26, v77
	v_med3_f32 v87, v87, s26, v77
	v_mov_b32_e32 v86, 0
	v_cvt_pk_fp8_f32 v86, v89, v87
	v_mul_f32_e32 v88, 0x42800000, v53
	v_mul_f32_e32 v87, 0x42800000, v61
	v_med3_f32 v88, v88, s26, v77
	v_med3_f32 v87, v87, s26, v77
	v_cvt_pk_fp8_f32 v86, v88, v87 op_sel:[0,0,1]
	v_mul_f32_e32 v87, 0x42800000, v45
	v_mul_f32_e32 v88, 0x42800000, v49
	v_med3_f32 v91, v87, s26, v77
	v_med3_f32 v88, v88, s26, v77
	v_mov_b32_e32 v87, 0
	v_cvt_pk_fp8_f32 v87, v91, v88
	v_mul_f32_e32 v89, 0x42800000, v37
	v_mul_f32_e32 v88, 0x42800000, v41
	v_med3_f32 v89, v89, s26, v77
	v_med3_f32 v88, v88, s26, v77
	v_cvt_pk_fp8_f32 v87, v89, v88 op_sel:[0,0,1]
	v_mul_f32_e32 v88, 0x42800000, v33
	v_mul_f32_e32 v89, 0x42800000, v29
	v_med3_f32 v92, v88, s26, v77
	v_med3_f32 v89, v89, s26, v77
	v_mov_b32_e32 v88, 0
	v_cvt_pk_fp8_f32 v88, v92, v89
	v_mul_f32_e32 v91, 0x42800000, v25
	v_mul_f32_e32 v89, 0x42800000, v21
	v_med3_f32 v91, v91, s26, v77
	v_med3_f32 v89, v89, s26, v77
	v_cvt_pk_fp8_f32 v88, v91, v89 op_sel:[0,0,1]
	v_mul_f32_e32 v89, 0x42800000, v17
	v_mul_f32_e32 v91, 0x42800000, v13
	v_med3_f32 v93, v89, s26, v77
	v_med3_f32 v91, v91, s26, v77
	v_mov_b32_e32 v89, 0
	v_cvt_pk_fp8_f32 v89, v93, v91
	v_mul_f32_e32 v92, 0x42800000, v9
	v_mul_f32_e32 v91, 0x42800000, v5
	v_med3_f32 v92, v92, s26, v77
	v_med3_f32 v91, v91, s26, v77
	v_cvt_pk_fp8_f32 v89, v92, v91 op_sel:[0,0,1]
	s_cmp_gt_u32 s27, 7
	ds_write_b128 v90, v[78:81] offset:144
	ds_write_b128 v90, v[82:85] offset:288
	ds_write_b128 v90, v[86:89] offset:432
	s_cbranch_scc1 .LBB0_664
	s_cmpk_gt_i32 s25, 0x1fff
	s_mov_b64 s[14:15], -1
	s_cbranch_scc0 .LBB0_668
	s_mov_b64 s[8:9], s[100:101]
	s_add_i32 s2, s25, 0xffffe000
	s_lshr_b32 s2, s2, 7
	s_lshl_b64 s[10:11], s[2:3], 24
	s_mov_b64 s[14:15], 0
	s_waitcnt lgkmcnt(0)
	s_add_u32 s8, s8, s10
	s_addc_u32 s9, s9, s11
	s_lshl_b64 s[10:11], s[2:3], 22
	s_add_u32 s10, s18, s10
	s_addc_u32 s11, s19, s11

; __device__ __forceinline__ void conv8_fill(const Ctx& X, int base, int rank, int nblk, int n) { conv8b_run(X, (base >> 3) + rank, nblk, n); }
; #define SEAM(k) do { if (IN(k) && IN((k) + 1)) xcd_barrier(bar); } while (0)
; __device__ __forceinline__ Cvb conv8b_dec(const Ctx& X, int bit) { Cvb c; int kb, nb;
;     if (bit < I_GU8 / 8) { const int e = bit >> 8, r = bit & 255; kb = r >> 4; nb = r & 15; c.N = 2 * DFF; c.W = XP_w_gu(X) + (size_t)e * D * (2 * DFF); c.WT = XP_WguT(X) + (size_t)e * 16 * PAN_GU + (size_t)kb * PAN_GU; }
;     else { const int b2 = bit - I_GU8 / 8, e = b2 >> 7, r = b2 & 127; kb = r >> 3; nb = r & 7; c.N = D; c.W = XP_w_d(X) + (size_t)e * DFF * D; c.WT = XP_WdT(X) + (size_t)e * 16 * PAN_D + (size_t)kb * PAN_D; }
;     c.W += (size_t)(kb * 128 + 16 * X.wave) * c.N + nb * 256 + 4 * X.lane;
;     c.WT += (size_t)(nb * 256 + 32 * X.wave + (X.lane >> 3)) * 128 + 16 * (X.lane & 7);
;     return c; }
; __global__ void __launch_bounds__(NTHR, 2) fwd(Args args) {
;     ...
;         const int gb = (X.G == 256) ? P5_GEMM_BLOCKS : X.G;
;         if (X.bid < gb) { DenseSched S{(const char*)XP_MIX(X), (const char*)XP_WoutT(X), 64, T / 256, D / 256, (T / 256) * (D / 256), gb, X.bid}; EpiOut E{XP_x(X), XP_Hh(X)};
;             pg8::gemm_phase<EpiOut, DenseSched, false, false>(X.lds, D, 64, 64, (size_t)PANE_A * 2, (size_t)PANE_WOUT * 2, S, E); }
;         else conv8_fill(X, Q5_BASE, X.bid - gb, Q5_W / NWAVES, Q5_N); } SEAM(5);
.LBB0_721:
	s_cmp_lt_i32 s94, 6
	s_cselect_b64 s[4:5], -1, 0
	s_and_b64 s[2:3], s[4:5], s[2:3]
	s_andn2_b64 vcc, exec, s[2:3]
	s_cbranch_vccnz .LBB0_762
	s_cmpk_lg_i32 s92, 0x100
	s_cselect_b32 s30, s92, 0x80
	s_cmp_ge_i32 s87, s30
	s_mov_b64 s[4:5], -1
	s_cbranch_scc0 .LBB0_737
	s_load_dwordx2 s[6:7], s[0:1], 0x70
	s_load_dwordx2 s[8:9], s[0:1], 0x80
	s_sub_i32 s18, s87, s30
	s_lshl_b32 s18, s18, 1
	s_add_i32 s18, s18, 0x1dc0
	s_mov_b32 s19, 26
	s_mov_b32 s24, 0xc3e00000
	v_mov_b32_e32 v150, 0x43e00000
	v_lshlrev_b32_e32 v146, 4, v194
	v_mul_u32_u24_e32 v147, 0x240, v194
	s_lshl_b32 s20, s93, 4
	v_add_u32_e32 v147, s20, v147
	v_lshrrev_b32_e32 v151, 3, v194
	s_lshl_b32 s20, s93, 5
	v_add_u32_e32 v152, s20, v151
	v_mul_u32_u24_e32 v148, 0x90, v152
	v_and_b32_e32 v152, 7, v194
	v_lshl_add_u32 v148, v152, 4, v148
	v_lshlrev_b32_e32 v151, 7, v151
	v_lshl_add_u32 v149, v152, 4, v151
	s_waitcnt lgkmcnt(0)
	s_add_i32 s27, s18, 1
	s_cmp_lt_u32 s18, 0x2000
	s_cbranch_scc0 .Lcv5_dnP0
	s_lshr_b32 s20, s18, 4
	s_lshl_b32 s20, s20, 21
	s_and_b32 s21, s18, 15
	s_lshl_b32 s21, s21, 10
	s_add_u32 s20, s20, s21
	s_lshl_b32 s21, s93, 18
	s_add_u32 s20, s20, s21
	s_add_u32 s10, s6, s20
	s_addc_u32 s11, s7, 0
	s_movk_i32 s12, 0x4000
	s_lshl_b32 s20, s18, 15
	s_add_u32 s20, s20, 0x30000000
	s_branch .Lcv5_cmP0
